# v28 + static s_setprio 1 for waves 4-7 while they run the steady-state MLA loop
# baseline (speedup 1.0000x reference)
; #define ISSUE_K(t, sl) do { glds16(Kg + (long)(t) * (KSLOT / 2), (unsigned)__builtin_amdgcn_readfirstlane(kdst + (sl) * KSLOT)); \
;         if (k2) glds16(Kg + (long)(t) * (KSLOT / 2) + 4096, (unsigned)__builtin_amdgcn_readfirstlane(kdst + (sl) * KSLOT + 8192)); } while (0)
; #define ISSUE_V(t, sl) glds16(Vg + (long)(t) * 4096, (unsigned)__builtin_amdgcn_readfirstlane(vdst + (sl) * VSLOT))
; #define SFENCE() __builtin_amdgcn_sched_barrier(0)
; template <bool FOX>
; __device__ __forceinline__ void attn_unit(const Args& A, int b, int h, int qb, LAS char* shm, LAS float* dg) {
;     ...
;     for (int t = 1; t < t_end; ++t) {
;         if (t == 1 && 4 < nti) ISSUE_K(t0 + 4, 0);
;         if (t + 4 < nti) ISSUE_K(t0 + t + 4, t % NS);
;         if (t + 2 < nti) ISSUE_V(t0 + t + 2, (t + 2) % NS);
;         SFENCE();
.LBB0_825:
	s_add_i32 s27, s26, 3
	s_cmp_lt_u32 s27, s94
	s_cbranch_scc0 .LBB0_828
	s_cmp_lg_u32 s98, 0
	s_cbranch_scc0 .Lmla_ss_no
	s_cmp_lg_u32 s26, s59
	s_cbranch_scc0 .Lmla_ss_no
	s_and_b32 s52, s27, 3
	s_mulk_i32 s52, 0x3000
	s_add_i32 s52, s52, s91
	s_add_i32 s53, s42, 0x6000
	s_and_b32 s53, s53, 0x6000
	s_add_i32 s53, s53, s93
	v_lshl_add_u64 v[250:251], v[232:233], 0, s[42:43]
	v_lshl_add_u64 v[240:241], v[234:235], 0, s[56:57]
	s_cmp_lt_i32 s89, 4
	s_cbranch_scc1 .Lmla_ss1_in
	s_setprio 1
	s_branch .Lmla_ss2_top

; #define ISSUE_K(t, sl) do { glds16(Kg + (long)(t) * (KSLOT / 2), (unsigned)__builtin_amdgcn_readfirstlane(kdst + (sl) * KSLOT)); \
;         if (k2) glds16(Kg + (long)(t) * (KSLOT / 2) + 4096, (unsigned)__builtin_amdgcn_readfirstlane(kdst + (sl) * KSLOT + 8192)); } while (0)
; #define ISSUE_V(t, sl) glds16(Vg + (long)(t) * 4096, (unsigned)__builtin_amdgcn_readfirstlane(vdst + (sl) * VSLOT))
; #define SFENCE() __builtin_amdgcn_sched_barrier(0)
; template <bool FOX>
; __device__ __forceinline__ void attn_unit(const Args& A, int b, int h, int qb, LAS char* shm, LAS float* dg) {
;     ...
;     for (int t = 1; t < t_end; ++t) {
;         if (t == 1 && 4 < nti) ISSUE_K(t0 + 4, 0);
;         if (t + 4 < nti) ISSUE_K(t0 + t + 4, t % NS);
;         if (t + 2 < nti) ISSUE_V(t0 + t + 2, (t + 2) % NS);
;         SFENCE();
.Lmla_ss_back:
	s_setprio 0
	s_waitcnt lgkmcnt(0)
	s_mov_b64 s[60:61], 0
	s_branch .LBB0_825
.Lmla_ss_done:
	s_setprio 0
	s_waitcnt lgkmcnt(0)
	s_mov_b64 s[46:47], -1
	s_mov_b64 s[52:53], -1
	s_mov_b64 s[60:61], 0
	s_branch .LBB0_867
